# static s_setprio 1 for waves 4-7 (younger half) during the MoE stream phases
# baseline (speedup 1.0000x reference)
; #define GAS __attribute__((address_space(1)))
; #define LAS __attribute__((address_space(3)))
;     unsigned char* ws = (unsigned char*)a.ws; LAS int* lc = (LAS int*)(lds + LDSCTL_OFF);
;     if (MODE == 0 || lw >= 0) moe_tables((const unsigned*)(ws + WS_CTL) + CW_CNT + l * 64 * 16, lc, tid);
;     if (lw >= 0) l = lw;
;     const size_t o_hid = out_off ? out_off : WS_HID, o_yr = out_off ? out_off : WS_YR;
;     constexpr int KD = (MODE == 0) ? D : DEXP, NT = KD / 64, NSLAB = (MODE == 0) ? 8 : 16, LDW = (MODE == 0) ? DEXP : D, LDX = KD;
;     const int half = wave & 1, nb16 = lane & 15, kb = 4 * (wave >> 1) + (lane >> 4);
;     const int tk = lane & 15, q = lane >> 4;
;     const GAS char* wmat = (const GAS char*)((MODE == 0) ? (half ? a.inp(I_WEU) : a.inp(I_WEG)) : a.inp(I_WED));
;     const unsigned wvo = (unsigned)((4 * kb * LDW + 4 * nb16) * 4);
;     const int lw0 = (64 * half + 4 * nb16) * 128 + (((kb >> 1) ^ ((2 * nb16) & 7)) << 4) + (kb & 1) * 8, lw1 = lw0 ^ 16;
;     const int rd_g = (tk >> 1) & 7;
.LBB0_1713:
	s_or_b64 exec, exec, s[12:13]
	s_cmpk_gt_i32 s3, 0x1ff
	s_waitcnt lgkmcnt(0)
	s_barrier
	s_cbranch_scc1 .LBB0_1727
	s_mov_b32 s83, 0
	s_mov_b32 s10, 0x7ffffff0
	s_ashr_i32 s12, s0, 6
	s_cmp_lt_u32 s12, 4
	s_cbranch_scc1 .Lprio_k
	s_setprio 1
.Lprio_k:
	s_and_b32 s7, s12, 1
	s_lshl_b32 s0, s12, 1
	v_bfe_u32 v4, v2, 4, 2
	v_and_or_b32 v5, s0, -4, v4
	s_cmp_eq_u32 s7, 0
	s_movk_i32 s0, 0xe8
	s_cselect_b32 s0, s0, 0xf0
	v_and_b32_e32 v3, 15, v2
	s_add_u32 s0, s4, s0
	s_addc_u32 s1, s5, 0
	s_waitcnt vmcnt(0)
	v_lshlrev_b32_e32 v6, 4, v3
	v_lshlrev_b32_e32 v90, 3, v4
	s_load_dwordx2 s[38:39], s[0:1], 0x0
	v_lshl_or_b32 v160, v5, 13, v6
	v_lshlrev_b32_e32 v6, 9, v3
	s_lshl_b32 s0, s7, 13
	v_and_b32_e32 v7, 8, v90
	v_or3_b32 v6, v7, v6, s0
	v_readlane_b32 s0, v255, 30
	s_lshl_b32 s24, s0, 6
	s_add_u32 s4, s8, 0x4300000
	v_lshrrev_b32_e32 v5, 1, v5
	v_lshlrev_b32_e32 v8, 1, v2
	s_addc_u32 s0, s9, 0
	v_bitop3_b32 v5, v5, v8, 6 bitop3:0x78
	s_and_b32 s5, s0, 0xffff
	s_mul_i32 s0, s12, 16
	s_mul_i32 s80, s12, 16
	v_bfe_u32 v8, v2, 3, 3
	v_or_b32_e32 v162, s0, v8
	v_lshlrev_b32_e32 v8, 4, v2
	v_and_b32_e32 v163, 0x70, v8
	v_bitop3_b32 v8, v4, v2, 7 bitop3:0x78
	v_lshl_add_u32 v161, v5, 4, v6
	v_lshrrev_b32_e32 v6, 1, v2
	v_bfe_u32 v7, v2, 1, 3
	s_add_u32 s25, s8, 0x39e61600
	s_mulk_i32 s12, 0x3000
	v_and_or_b32 v2, v2, 56, v8
	v_readlane_b32 s1, v255, 31
	s_addc_u32 s26, s9, 0
	s_add_i32 s27, s12, 0
	v_lshlrev_b32_e32 v172, 4, v2
	v_lshlrev_b32_e32 v2, 7, v3
	v_add_u32_e32 v173, s27, v2
	v_add_u32_e32 v176, 0, v2
	v_or_b32_e32 v177, s0, v3
	v_lshl_add_u64 v[2:3], s[8:9], 0, v[90:91]
	s_mov_b64 s[0:1], 0x2fe31000
	v_xor_b32_e32 v5, 16, v161
	v_bitop3_b32 v6, v6, v4, 7 bitop3:0x6c
	v_bitop3_b32 v4, v4, v7, 4 bitop3:0x36
	v_lshl_add_u64 v[156:157], v[2:3], 0, s[0:1]
	v_xor_b32_e32 v2, 64, v172
	s_mov_b32 s7, s11
	v_lshlrev_b32_e32 v174, 4, v6
	v_lshlrev_b32_e32 v175, 4, v4
	v_or_b32_e32 v90, 0x800, v160
	v_or_b32_e32 v178, 0x1000, v160
	v_or_b32_e32 v179, 0x1800, v160
	v_add_u32_e32 v180, 0, v5
	v_add_u32_e32 v181, s27, v2
	s_branch .LBB0_1716

; #define GAS __attribute__((address_space(1)))
; #define LAS __attribute__((address_space(3)))
;     ...
;     for (int vb = bid; vb < NEXP * NSLAB; vb += G) {
;         const int xcd = vb & 7, idx = vb >> 3; const int e = xcd * 8 + idx / NSLAB, slab = idx % NSLAB;
;         const int M = __builtin_amdgcn_readfirstlane(lc[LC_CNT / 4 + e]), row0 = __builtin_amdgcn_readfirstlane(lc[LC_PSTART / 4 + e]);
;         const size_t wuo = (MODE == 0) ? ((size_t)(l * NEXP + e) * D * DEXP + slab * 64) * 4 : ((size_t)(l * NEXP + e) * DEXP * D + slab * 128 + 64 * half) * 4;
;         const __amdgpu_buffer_rsrc_t wrs = __builtin_amdgcn_make_buffer_rsrc((void*)(wmat + wuo), 0, KD * LDW * 4, 0x00020000);
;         const __amdgpu_buffer_rsrc_t xrs = __builtin_amdgcn_make_buffer_rsrc((MODE == 0) ? (void*)(ws + WS_U) : (void*)((const GAS char*)(ws + WS_HID) + (size_t)row0 * LDX * 2), 0, 0x7fffffff, 0x00020000);
;         const int* el = (const int*)(ws + WS_ELIST) + (size_t)e * T;
;         for (int rp = 0; rp < M; rp += 384) {
;             unsigned xso[6];
; #pragma unroll
;             for (int i = 0; i < 6; ++i) { int tok = rp + wave * 48 + 8 * i + (lane >> 3); tok = min(tok, M - 1); if (VAR == 5) tok &= 15; if (MODE == 0) tok = el[tok]; xso[i] = (unsigned)(tok * LDX * 2 + (lane & 7) * 16); }
;             LAS unsigned char* xw = lds + MS_XOFF + wave * MS_XWAVE; const int xwo = (lane >> 3) * 128 + (((lane & 7) ^ ((lane >> 4) & 3)) << 4);
;             const LAS unsigned char* xr = lds + MS_XOFF + wave * MS_XWAVE + tk * 128 + ((q ^ rd_g) << 4);
;             f32x4 acc[3][8];
; #pragma unroll
;             for (int mt = 0; mt < 3; ++mt)
; #pragma unroll
;                 for (int j = 0; j < 8; ++j) acc[mt][j] = (f32x4){0.f, 0.f, 0.f, 0.f};
;             f32x4 wr[2][4];
;             bf16x8 xs[6];
.LBB0_1727:
	s_setprio 0
	s_mov_b32 s67, 0
	s_mov_b32 s10, 0x400000
	v_readlane_b32 s0, v255, 32
	s_add_i32 s0, s0, 10
	s_cmp_ge_i32 s0, s77
	s_cbranch_scc1 .LBB0_1777
	s_waitcnt vmcnt(0)
	s_barrier
	v_readfirstlane_b32 s88, v0
	s_lshr_b32 s88, s88, 6
	s_cmp_eq_u32 s88, 0
	s_cbranch_scc1 .Lpfl_end
	s_cmpk_gt_i32 s72, 0x3ff
	s_cbranch_scc1 .Lpfl_end
	s_load_dwordx2 s[70:71], s[74:75], 0xf8
	v_readlane_b32 s82, v255, 30
	s_lshl_b32 s82, s82, 6
	s_and_b32 s84, s72, 7
	s_lshl_b32 s84, s84, 3
	s_lshr_b32 s85, s72, 7
	s_add_i32 s84, s84, s85
	s_add_i32 s84, s84, s82
	s_lshr_b32 s85, s72, 3
	s_and_b32 s85, s85, 15
	s_lshl_b32 s85, s85, 9
	s_and_b32 s81, s88, 1
	s_lshl_b32 s81, s81, 8
	s_or_b32 s85, s85, s81
	s_lshr_b32 s86, s84, 10
	s_lshl_b32 s84, s84, 22
	s_or_b32 s84, s84, s85
	s_waitcnt lgkmcnt(0)
	s_add_u32 s84, s70, s84
	s_addc_u32 s85, s71, s86
	s_and_b32 s85, s85, 0xffff
	s_mov_b32 s86, 0x7ffffff0
	s_mov_b32 s87, 0x20000
	v_and_b32_e32 v250, 15, v0
	v_lshlrev_b32_e32 v250, 4, v250
	v_bfe_u32 v251, v0, 4, 2
	s_lshr_b32 s81, s88, 1
	s_lshl_b32 s81, s81, 2
	v_add_u32_e32 v251, s81, v251
	v_lshl_or_b32 v250, v251, 15, v250
	v_or_b32_e32 v251, 0x2000, v250
	v_or_b32_e32 v252, 0x4000, v250
	v_or_b32_e32 v253, 0x6000, v250
	buffer_load_dwordx4 v[52:55], v250, s[84:87], 0 offen nt
	buffer_load_dwordx4 v[56:59], v251, s[84:87], 0 offen nt
	buffer_load_dwordx4 v[60:63], v252, s[84:87], 0 offen nt
	buffer_load_dwordx4 v[64:67], v253, s[84:87], 0 offen nt
	s_mov_b32 s81, 0x80000
	buffer_load_dwordx4 v[120:123], v250, s[84:87], s81 offen nt
	buffer_load_dwordx4 v[128:131], v251, s[84:87], s81 offen nt
	buffer_load_dwordx4 v[124:127], v252, s[84:87], s81 offen nt
	buffer_load_dwordx4 v[132:135], v253, s[84:87], s81 offen nt
	s_mov_b32 s81, 0x100000
	buffer_load_dwordx4 v[136:139], v250, s[84:87], s81 offen nt
	buffer_load_dwordx4 v[140:143], v251, s[84:87], s81 offen nt
	buffer_load_dwordx4 v[144:147], v252, s[84:87], s81 offen nt
	buffer_load_dwordx4 v[148:151], v253, s[84:87], s81 offen nt
	s_mov_b32 s67, 1

; #define GAS __attribute__((address_space(1)))
; #define LAS __attribute__((address_space(3)))
;     unsigned char* ws = (unsigned char*)a.ws; LAS int* lc = (LAS int*)(lds + LDSCTL_OFF);
;     if (MODE == 0 || lw >= 0) moe_tables((const unsigned*)(ws + WS_CTL) + CW_CNT + l * 64 * 16, lc, tid);
;     if (lw >= 0) l = lw;
;     const size_t o_hid = out_off ? out_off : WS_HID, o_yr = out_off ? out_off : WS_YR;
;     constexpr int KD = (MODE == 0) ? D : DEXP, NT = KD / 64, NSLAB = (MODE == 0) ? 8 : 16, LDW = (MODE == 0) ? DEXP : D, LDX = KD;
;     const int half = wave & 1, nb16 = lane & 15, kb = 4 * (wave >> 1) + (lane >> 4);
;     const int tk = lane & 15, q = lane >> 4;
;     const GAS char* wmat = (const GAS char*)((MODE == 0) ? (half ? a.inp(I_WEU) : a.inp(I_WEG)) : a.inp(I_WED));
;     const unsigned wvo = (unsigned)((4 * kb * LDW + 4 * nb16) * 4);
;     const int lw0 = (64 * half + 4 * nb16) * 128 + (((kb >> 1) ^ ((2 * nb16) & 7)) << 4) + (kb & 1) * 8, lw1 = lw0 ^ 16;
;     const int rd_g = (tk >> 1) & 7;
.LBB0_1778:
	s_mov_b32 s83, 0
	s_mov_b32 s10, 0x7ffffff0
	s_waitcnt vmcnt(7)
	v_mov_b32_e32 v2, v0
	s_load_dwordx4 s[0:3], s[74:75], 0x108
	s_mov_b64 s[4:5], s[74:75]
	s_waitcnt lgkmcnt(0)
	s_load_dword s0, s[78:79], 0x0
	s_mov_b32 s1, s72
	s_waitcnt lgkmcnt(0)
	s_cmpk_gt_i32 s1, 0x3ff
	v_readfirstlane_b32 s7, v2
	s_cbranch_scc1 .LBB0_1792
	s_ashr_i32 s8, s7, 6
	s_cmp_lt_u32 s8, 4
	s_cbranch_scc1 .Lprio_l
	s_setprio 1
.Lprio_l:
	s_load_dwordx2 s[12:13], s[4:5], 0xf8
	v_and_b32_e32 v3, 15, v2
	s_lshl_b32 s4, s8, 1
	v_bfe_u32 v4, v2, 4, 2
	v_and_or_b32 v5, s4, -4, v4
	s_waitcnt vmcnt(0)
	v_lshlrev_b32_e32 v6, 4, v3
	s_and_b32 s94, s7, 64
	v_lshlrev_b32_e32 v90, 3, v4
	v_lshl_or_b32 v160, v5, 15, v6
	v_lshlrev_b32_e32 v6, 9, v3
	s_lshl_b32 s4, s94, 7
	v_and_b32_e32 v7, 8, v90
	v_or3_b32 v6, s4, v6, v7
	v_readlane_b32 s4, v255, 30
	s_lshl_b32 s26, s4, 6
	s_mul_i32 s4, s8, 16
	s_mul_i32 s80, s8, 16
	v_bfe_u32 v8, v2, 3, 3
	v_lshrrev_b32_e32 v5, 1, v5
	v_lshlrev_b32_e32 v7, 1, v2
	v_or_b32_e32 v162, s4, v8
	v_lshlrev_b32_e32 v8, 4, v2
	v_bitop3_b32 v5, v5, v7, 6 bitop3:0x78
	v_and_b32_e32 v163, 0x70, v8
	v_bitop3_b32 v8, v4, v2, 7 bitop3:0x78
	v_lshl_add_u32 v161, v5, 4, v6
	v_lshrrev_b32_e32 v6, 1, v2
	v_bfe_u32 v7, v2, 1, 3
	s_add_u32 s27, s2, 0x2fe31000
	s_mulk_i32 s8, 0x3000
	v_and_or_b32 v2, v2, 56, v8
	s_addc_u32 s28, s3, 0
	s_add_i32 s29, s8, 0
	v_lshlrev_b32_e32 v172, 4, v2
	v_lshlrev_b32_e32 v2, 7, v3
	v_add_u32_e32 v173, s29, v2
	v_add_u32_e32 v176, 0, v2
	v_or_b32_e32 v177, s4, v3
	v_lshl_add_u64 v[2:3], s[2:3], 0, v[90:91]
	s_mov_b64 s[2:3], 0x31e31000
	v_xor_b32_e32 v5, 16, v161
	v_bitop3_b32 v6, v6, v4, 7 bitop3:0x6c
	v_bitop3_b32 v4, v4, v7, 4 bitop3:0x36
	v_lshl_add_u64 v[156:157], v[2:3], 0, s[2:3]
	v_xor_b32_e32 v2, 64, v172
	v_lshlrev_b32_e32 v174, 4, v6
	v_lshlrev_b32_e32 v175, 4, v4
	v_or_b32_e32 v90, 0x2000, v160
	v_or_b32_e32 v178, 0x4000, v160
	v_or_b32_e32 v179, 0x6000, v160
	v_add_u32_e32 v180, 0, v5
	v_add_u32_e32 v181, s29, v2
	v_readlane_b32 s5, v255, 31
	s_branch .LBB0_1781

; #define IN(k) (((PHMASK >> PHBIT(k)) & 1u) && lo <= (k) && (k) < hi)
; #define SEAM(k) do { if (IN(k) && IN((k) + 1)) xcd_barrier(bar); } while (0)
; #define DUP(bit) if constexpr (((PROBE_DUP >> (bit)) & 1u) != 0u)
; __global__ void __launch_bounds__(NTHR, 2) mk_fwd(ArgsV argsv) {
;     ...
;         if (IN(pb + 9)) { { PH_BEGIN(); moe_stream_phase<1>(a, l, lds, wave, lane, tid, bid, G); } DUP(PB_MOEL) { PH_BEGIN(); moe_stream_phase<1>(a, l, lds, wave, lane, tid, bid, G); }
;             DUP(PB_MOEL_COLD) { PH_BEGIN(); moe_stream_phase<1>(a, l, lds, wave, lane, tid, bid, G, 1 - l, WS_XR); } } SEAM(pb + 9);
.LBB0_1792:
	s_setprio 0
	s_mov_b32 s10, 0x400000
	v_readlane_b32 s0, v255, 32
	s_add_i32 s0, s0, 11
	s_cmp_ge_i32 s0, s77
	s_cbranch_scc0 .LBB0_1793
	s_getpc_b64 s[98:99]
